# P11: next token's route records loaded one token ahead (v232..v246), record waits removed
# baseline (speedup 1.0000x reference)
.LBB0_1504:
	s_ashr_i32 s0, s4, 6
	v_readlane_b32 s1, v255, 16
	s_add_i32 s8, s0, s1
	s_cmpk_gt_i32 s8, 0x3fff
	s_cbranch_scc1 .LBB0_1507
	v_lshlrev_b32_e32 v1, 3, v0
	s_waitcnt vmcnt(0)
	v_and_b32_e32 v8, 0x1f8, v1
	v_mbcnt_lo_u32_b32 v1, -1, 0
	v_mbcnt_hi_u32_b32 v1, -1, v1
	v_and_b32_e32 v3, 64, v1
	v_add_u32_e32 v3, 64, v3
	v_xor_b32_e32 v4, 1, v1
	v_cmp_lt_i32_e32 vcc, v4, v3
	s_load_dwordx4 s[4:7], s[90:91], 0xf0
	s_add_u32 s10, s2, 0x44000000
	v_cndmask_b32_e32 v4, v1, v4, vcc
	v_lshlrev_b32_e32 v21, 2, v4
	v_xor_b32_e32 v4, 2, v1
	v_cmp_lt_i32_e32 vcc, v4, v3
	v_mov_b32_e32 v9, 0
	s_addc_u32 s11, s3, 0
	v_cndmask_b32_e32 v4, v1, v4, vcc
	v_lshlrev_b32_e32 v23, 2, v4
	v_xor_b32_e32 v4, 4, v1
	v_cmp_lt_i32_e32 vcc, v4, v3
	v_lshlrev_b32_e32 v2, 2, v8
	s_ashr_i32 s9, s8, 31
	v_cndmask_b32_e32 v4, v1, v4, vcc
	v_lshlrev_b32_e32 v25, 2, v4
	v_xor_b32_e32 v4, 8, v1
	v_cmp_lt_i32_e32 vcc, v4, v3
	v_mov_b32_e32 v5, v9
	s_lshl_b64 s[0:1], s[8:9], 12
	v_cndmask_b32_e32 v4, v1, v4, vcc
	v_lshlrev_b32_e32 v27, 2, v4
	v_xor_b32_e32 v4, 16, v1
	v_cmp_lt_i32_e32 vcc, v4, v3
	v_and_b32_e32 v0, 63, v0
	s_ashr_i32 s75, s74, 31
	v_cndmask_b32_e32 v4, v1, v4, vcc
	v_lshlrev_b32_e32 v28, 2, v4
	v_xor_b32_e32 v4, 32, v1
	v_cmp_lt_i32_e32 vcc, v4, v3
	v_mov_b32_e32 v3, v9
	s_waitcnt lgkmcnt(0)
	v_lshl_add_u64 v[10:11], s[4:5], 0, v[2:3]
	v_cndmask_b32_e32 v1, v1, v4, vcc
	v_or_b32_e32 v4, 0x1000, v2
	v_or_b32_e32 v2, 0x1800, v2
	v_lshl_add_u64 v[12:13], s[4:5], 0, v[4:5]
	v_lshl_add_u64 v[14:15], s[4:5], 0, v[2:3]
	v_lshl_or_b32 v16, v0, 4, s0
	v_mov_b32_e32 v17, s1
	s_lshl_b64 s[4:5], s[74:75], 12
	s_lshl_b64 s[0:1], s[8:9], 13
	s_add_u32 s0, s6, s0
	v_lshlrev_b32_e32 v29, 2, v1
	v_lshlrev_b32_e32 v0, 5, v0
	v_mov_b32_e32 v1, v9
	s_addc_u32 s1, s7, s1
	v_lshl_add_u64 v[0:1], s[0:1], 0, v[0:1]
	s_mov_b64 s[0:1], 0x1000
	v_lshl_add_u64 v[18:19], v[0:1], 0, s[0:1]
	s_lshl_b64 s[6:7], s[74:75], 13
	s_lshl_b64 s[12:13], s[8:9], 6
	s_lshl_b64 s[14:15], s[74:75], 6
	v_mov_b32_e32 v30, 0x5e30000
	s_add_i32 s9, 0, 0x21040
	v_mov_b32_e32 v31, 0x3727c5ac
	s_mov_b32 s16, 0xf800000
	v_mov_b32_e32 v32, 0x260
	global_load_dwordx4 v[200:203], v[10:11], off offset:16
	global_load_dwordx4 v[204:207], v[10:11], off
	global_load_dwordx4 v[208:211], v[10:11], off offset:2048
	global_load_dwordx4 v[212:215], v[10:11], off offset:2064
	global_load_dwordx4 v[216:219], v[12:13], off
	global_load_dwordx4 v[220:223], v[12:13], off offset:16
	global_load_dwordx4 v[224:227], v[14:15], off
	global_load_dwordx4 v[228:231], v[14:15], off offset:16
	s_add_u32 s0, s2, s12
	s_addc_u32 s1, s3, s13
	global_load_dwordx3 v[232:234], v30, s[0:1]
	global_load_dwordx3 v[236:238], v30, s[0:1] offset:16
	global_load_dwordx3 v[240:242], v30, s[0:1] offset:32
	global_load_dwordx3 v[244:246], v30, s[0:1] offset:48
	s_waitcnt vmcnt(0)
.LBB0_1506:
	s_add_u32 s0, s2, s12
	s_addc_u32 s1, s3, s13
	s_add_u32 s0, s0, s14
	s_addc_u32 s1, s1, s15
	v_mov_b32_e32 v0, v200
	v_mov_b32_e32 v1, v201
	v_mov_b32_e32 v2, v202
	v_mov_b32_e32 v3, v203
	v_mov_b32_e32 v4, v204
	v_mov_b32_e32 v5, v205
	v_mov_b32_e32 v6, v206
	v_mov_b32_e32 v7, v207
	v_mov_b32_e32 v50, v232
	v_mov_b32_e32 v51, v233
	v_mov_b32_e32 v52, v234
	v_mov_b32_e32 v54, v236
	v_mov_b32_e32 v55, v237
	v_mov_b32_e32 v56, v238
	v_mov_b32_e32 v58, v240
	v_mov_b32_e32 v59, v241
	v_mov_b32_e32 v60, v242
	v_mov_b32_e32 v62, v244
	v_mov_b32_e32 v63, v245
	v_mov_b32_e32 v64, v246
	global_load_dwordx3 v[232:234], v30, s[0:1]
	global_load_dwordx3 v[236:238], v30, s[0:1] offset:16
	global_load_dwordx3 v[240:242], v30, s[0:1] offset:32
	global_load_dwordx3 v[244:246], v30, s[0:1] offset:48
	v_lshl_add_u64 v[34:35], s[2:3], 0, v[16:17]
	v_add_co_u32_e32 v66, vcc, 0x22000000, v34
	s_add_i32 s8, s8, s74
	s_nop 0
	v_addc_co_u32_e32 v67, vcc, 0, v35, vcc
	global_load_dwordx4 v[34:37], v[66:67], off offset:3072
	global_load_dwordx4 v[38:41], v[66:67], off
	global_load_dwordx4 v[42:45], v[66:67], off offset:1024
	global_load_dwordx4 v[46:49], v[66:67], off offset:2048
	s_add_u32 s12, s12, s14
	s_addc_u32 s13, s13, s15
	v_lshl_add_u64 v[16:17], v[16:17], 0, s[4:5]
	s_cmpk_lt_i32 s8, 0x4000
	s_nop 0
	v_lshlrev_b32_e32 v33, 2, v50
	s_nop 0
	v_lshlrev_b32_e32 v57, 2, v54
	s_nop 0
	v_lshlrev_b32_e32 v61, 2, v58
	s_nop 0
	v_lshlrev_b32_e32 v62, 2, v62
	v_add_u32_e32 v33, s9, v33
	v_add_u32_e32 v75, s9, v57
	v_add_u32_e32 v77, s9, v61
	v_add_u32_e32 v79, s9, v62
	ds_read_b32 v74, v33
	ds_read_b32 v76, v75
	ds_read_b32 v78, v77
	ds_read_b32 v80, v79
	v_ashrrev_i32_e32 v67, 31, v51
	s_waitcnt lgkmcnt(3)
	v_ashrrev_i32_e32 v75, 31, v74
	s_waitcnt lgkmcnt(2)
	v_ashrrev_i32_e32 v77, 31, v76
	v_mov_b32_e32 v66, v51
	v_ashrrev_i32_e32 v51, 31, v55
	v_mov_b32_e32 v50, v55
	s_waitcnt lgkmcnt(1)
	v_ashrrev_i32_e32 v79, 31, v78
	s_waitcnt lgkmcnt(0)
	v_ashrrev_i32_e32 v81, 31, v80
	v_lshlrev_b64 v[74:75], 19, v[74:75]
	v_lshlrev_b64 v[76:77], 19, v[76:77]
	v_ashrrev_i32_e32 v55, 31, v59
	v_mov_b32_e32 v54, v59
	v_ashrrev_i32_e32 v59, 31, v63
	v_mov_b32_e32 v58, v63
	v_mov_b32_e32 v26, v52
	v_lshlrev_b64 v[52:53], 11, v[66:67]
	v_lshlrev_b64 v[50:51], 11, v[50:51]
	v_lshlrev_b64 v[78:79], 19, v[78:79]
	v_lshlrev_b64 v[80:81], 19, v[80:81]
	v_lshl_add_u64 v[74:75], s[10:11], 0, v[74:75]
	v_lshl_add_u64 v[76:77], s[10:11], 0, v[76:77]
	v_mov_b32_e32 v24, v56
	v_lshlrev_b64 v[54:55], 11, v[54:55]
	v_lshlrev_b64 v[56:57], 11, v[58:59]
	v_lshl_add_u64 v[78:79], s[10:11], 0, v[78:79]
	v_lshl_add_u64 v[80:81], s[10:11], 0, v[80:81]
	v_lshl_add_u64 v[52:53], v[74:75], 0, v[52:53]
	v_lshl_add_u64 v[50:51], v[76:77], 0, v[50:51]
	v_lshl_add_u64 v[54:55], v[78:79], 0, v[54:55]
	v_lshl_add_u64 v[56:57], v[80:81], 0, v[56:57]
	v_lshl_add_u64 v[52:53], v[52:53], 0, v[8:9]
	v_lshl_add_u64 v[50:51], v[50:51], 0, v[8:9]
	v_lshl_add_u64 v[54:55], v[54:55], 0, v[8:9]
	v_lshl_add_u64 v[56:57], v[56:57], 0, v[8:9]
	global_load_dwordx2 v[74:75], v[52:53], off
	global_load_dwordx2 v[76:77], v[52:53], off offset:512
	global_load_dwordx2 v[78:79], v[52:53], off offset:1024
	global_load_dwordx2 v[80:81], v[52:53], off offset:1536
	global_load_dwordx2 v[82:83], v[50:51], off
	global_load_dwordx2 v[84:85], v[50:51], off offset:512
	global_load_dwordx2 v[86:87], v[50:51], off offset:1024
	global_load_dwordx2 v[88:89], v[50:51], off offset:1536
	global_load_dwordx2 v[90:91], v[54:55], off
	global_load_dwordx2 v[92:93], v[54:55], off offset:512
	global_load_dwordx2 v[94:95], v[54:55], off offset:1024
	global_load_dwordx2 v[96:97], v[54:55], off offset:1536
	global_load_dwordx2 v[98:99], v[56:57], off
	global_load_dwordx2 v[100:101], v[56:57], off offset:512
	global_load_dwordx2 v[102:103], v[56:57], off offset:1024
	global_load_dwordx2 v[50:51], v[56:57], off offset:1536
	s_waitcnt vmcnt(18)
	v_cvt_f32_f16_e32 v62, v38
	v_cvt_f32_f16_sdwa v63, v38 dst_sel:DWORD dst_unused:UNUSED_PAD src0_sel:WORD_1
	v_cvt_f32_f16_e32 v38, v39
	v_cvt_f32_f16_sdwa v39, v39 dst_sel:DWORD dst_unused:UNUSED_PAD src0_sel:WORD_1
	v_mov_b32_e32 v22, v60
	v_mov_b32_e32 v20, v64
	v_cvt_f32_f16_e32 v58, v37
	v_cvt_f32_f16_sdwa v59, v37 dst_sel:DWORD dst_unused:UNUSED_PAD src0_sel:WORD_1
	v_cvt_f32_f16_e32 v60, v40
	v_cvt_f32_f16_sdwa v61, v40 dst_sel:DWORD dst_unused:UNUSED_PAD src0_sel:WORD_1
	v_cvt_f32_f16_e32 v40, v41
	v_cvt_f32_f16_sdwa v41, v41 dst_sel:DWORD dst_unused:UNUSED_PAD src0_sel:WORD_1
	s_waitcnt vmcnt(17)
	v_cvt_f32_f16_e32 v64, v44
	v_cvt_f32_f16_sdwa v65, v44 dst_sel:DWORD dst_unused:UNUSED_PAD src0_sel:WORD_1
	v_cvt_f32_f16_e32 v44, v45
	v_cvt_f32_f16_sdwa v45, v45 dst_sel:DWORD dst_unused:UNUSED_PAD src0_sel:WORD_1
	v_cvt_f32_f16_e32 v66, v42
	v_cvt_f32_f16_sdwa v67, v42 dst_sel:DWORD dst_unused:UNUSED_PAD src0_sel:WORD_1
	v_cvt_f32_f16_e32 v42, v43
	v_cvt_f32_f16_sdwa v43, v43 dst_sel:DWORD dst_unused:UNUSED_PAD src0_sel:WORD_1
	s_waitcnt vmcnt(16)
	v_cvt_f32_f16_e32 v68, v48
	v_cvt_f32_f16_sdwa v69, v48 dst_sel:DWORD dst_unused:UNUSED_PAD src0_sel:WORD_1
	v_cvt_f32_f16_e32 v48, v49
	v_cvt_f32_f16_sdwa v49, v49 dst_sel:DWORD dst_unused:UNUSED_PAD src0_sel:WORD_1
	v_cvt_f32_f16_e32 v70, v46
	v_cvt_f32_f16_sdwa v71, v46 dst_sel:DWORD dst_unused:UNUSED_PAD src0_sel:WORD_1
	v_cvt_f32_f16_e32 v46, v47
	v_cvt_f32_f16_sdwa v47, v47 dst_sel:DWORD dst_unused:UNUSED_PAD src0_sel:WORD_1
	v_cvt_f32_f16_e32 v72, v36
	v_cvt_f32_f16_sdwa v73, v36 dst_sel:DWORD dst_unused:UNUSED_PAD src0_sel:WORD_1
	v_cvt_f32_f16_e32 v36, v34
	v_cvt_f32_f16_sdwa v37, v34 dst_sel:DWORD dst_unused:UNUSED_PAD src0_sel:WORD_1
	v_cvt_f32_f16_e32 v34, v35
	v_cvt_f32_f16_sdwa v35, v35 dst_sel:DWORD dst_unused:UNUSED_PAD src0_sel:WORD_1
	s_waitcnt vmcnt(15)
	v_cvt_pk_f32_fp8_e32 v[52:53], v74
	v_cvt_pk_f32_fp8_sdwa v[54:55], v74 src0_sel:WORD_1
	v_cvt_pk_f32_fp8_e32 v[56:57], v75
	v_cvt_pk_f32_fp8_sdwa v[74:75], v75 src0_sel:WORD_1
	s_waitcnt vmcnt(11)
	v_cvt_pk_f32_fp8_e32 v[122:123], v82
	v_cvt_pk_f32_fp8_e32 v[104:105], v76
	v_cvt_pk_f32_fp8_sdwa v[106:107], v76 src0_sel:WORD_1
	v_cvt_pk_f32_fp8_e32 v[108:109], v77
	v_cvt_pk_f32_fp8_sdwa v[76:77], v77 src0_sel:WORD_1
	v_cvt_pk_f32_fp8_e32 v[110:111], v78
	v_cvt_pk_f32_fp8_sdwa v[112:113], v78 src0_sel:WORD_1
	v_cvt_pk_f32_fp8_e32 v[114:115], v79
	v_cvt_pk_f32_fp8_sdwa v[78:79], v79 src0_sel:WORD_1
	v_cvt_pk_f32_fp8_e32 v[116:117], v80
	v_cvt_pk_f32_fp8_sdwa v[118:119], v80 src0_sel:WORD_1
	v_cvt_pk_f32_fp8_e32 v[120:121], v81
	v_cvt_pk_f32_fp8_sdwa v[80:81], v81 src0_sel:WORD_1
	v_cvt_pk_f32_fp8_sdwa v[124:125], v82 src0_sel:WORD_1
	s_waitcnt vmcnt(7)
	v_cvt_pk_f32_fp8_e32 v[146:147], v90
	v_cvt_pk_f32_fp8_e32 v[126:127], v83
	v_cvt_pk_f32_fp8_sdwa v[82:83], v83 src0_sel:WORD_1
	v_cvt_pk_f32_fp8_e32 v[128:129], v84
	v_cvt_pk_f32_fp8_sdwa v[130:131], v84 src0_sel:WORD_1
	v_cvt_pk_f32_fp8_e32 v[132:133], v85
	v_cvt_pk_f32_fp8_sdwa v[84:85], v85 src0_sel:WORD_1
	v_cvt_pk_f32_fp8_e32 v[134:135], v86
	v_cvt_pk_f32_fp8_sdwa v[136:137], v86 src0_sel:WORD_1
	v_cvt_pk_f32_fp8_e32 v[138:139], v87
	v_cvt_pk_f32_fp8_sdwa v[86:87], v87 src0_sel:WORD_1
	v_cvt_pk_f32_fp8_e32 v[140:141], v88
	v_cvt_pk_f32_fp8_sdwa v[142:143], v88 src0_sel:WORD_1
	v_cvt_pk_f32_fp8_e32 v[144:145], v89
	v_cvt_pk_f32_fp8_sdwa v[88:89], v89 src0_sel:WORD_1
	v_cvt_pk_f32_fp8_sdwa v[148:149], v90 src0_sel:WORD_1
	s_waitcnt vmcnt(3)
	v_cvt_pk_f32_fp8_e32 v[170:171], v98
	v_cvt_pk_f32_fp8_e32 v[150:151], v91
	v_cvt_pk_f32_fp8_sdwa v[90:91], v91 src0_sel:WORD_1
	v_cvt_pk_f32_fp8_e32 v[152:153], v92
	v_cvt_pk_f32_fp8_sdwa v[154:155], v92 src0_sel:WORD_1
	v_cvt_pk_f32_fp8_e32 v[156:157], v93
	v_cvt_pk_f32_fp8_sdwa v[92:93], v93 src0_sel:WORD_1
	v_cvt_pk_f32_fp8_e32 v[158:159], v94
	v_cvt_pk_f32_fp8_sdwa v[160:161], v94 src0_sel:WORD_1
	v_cvt_pk_f32_fp8_e32 v[162:163], v95
	v_cvt_pk_f32_fp8_sdwa v[94:95], v95 src0_sel:WORD_1
	v_cvt_pk_f32_fp8_e32 v[164:165], v96
	v_cvt_pk_f32_fp8_sdwa v[166:167], v96 src0_sel:WORD_1
	v_cvt_pk_f32_fp8_e32 v[168:169], v97
	v_cvt_pk_f32_fp8_sdwa v[96:97], v97 src0_sel:WORD_1
	v_cvt_pk_f32_fp8_sdwa v[172:173], v98 src0_sel:WORD_1
	v_pk_fma_f32 v[52:53], v[26:27], v[52:53], v[62:63] op_sel_hi:[0,1,1]
	v_cvt_pk_f32_fp8_e32 v[174:175], v99
	v_cvt_pk_f32_fp8_sdwa v[98:99], v99 src0_sel:WORD_1
	s_waitcnt vmcnt(2)
	v_cvt_pk_f32_fp8_e32 v[176:177], v100
	v_cvt_pk_f32_fp8_sdwa v[178:179], v100 src0_sel:WORD_1
	v_cvt_pk_f32_fp8_e32 v[180:181], v101
	v_cvt_pk_f32_fp8_sdwa v[100:101], v101 src0_sel:WORD_1
	s_waitcnt vmcnt(1)
	v_cvt_pk_f32_fp8_e32 v[182:183], v102
	v_cvt_pk_f32_fp8_sdwa v[184:185], v102 src0_sel:WORD_1
	v_cvt_pk_f32_fp8_e32 v[186:187], v103
	v_cvt_pk_f32_fp8_sdwa v[102:103], v103 src0_sel:WORD_1
	s_waitcnt vmcnt(0)
	v_cvt_pk_f32_fp8_e32 v[188:189], v50
	v_cvt_pk_f32_fp8_sdwa v[190:191], v50 src0_sel:WORD_1
	v_cvt_pk_f32_fp8_e32 v[192:193], v51
	v_cvt_pk_f32_fp8_sdwa v[50:51], v51 src0_sel:WORD_1
	v_pk_fma_f32 v[38:39], v[26:27], v[54:55], v[38:39] op_sel_hi:[0,1,1]
	v_pk_fma_f32 v[52:53], v[24:25], v[122:123], v[52:53] op_sel_hi:[0,1,1]
	v_pk_fma_f32 v[58:59], v[26:27], v[80:81], v[58:59] op_sel_hi:[0,1,1]
	v_pk_fma_f32 v[56:57], v[26:27], v[56:57], v[60:61] op_sel_hi:[0,1,1]
	v_pk_fma_f32 v[40:41], v[26:27], v[74:75], v[40:41] op_sel_hi:[0,1,1]
	v_pk_fma_f32 v[54:55], v[26:27], v[108:109], v[64:65] op_sel_hi:[0,1,1]
	v_pk_fma_f32 v[44:45], v[26:27], v[76:77], v[44:45] op_sel_hi:[0,1,1]
	v_pk_fma_f32 v[60:61], v[26:27], v[104:105], v[66:67] op_sel_hi:[0,1,1]
	v_pk_fma_f32 v[42:43], v[26:27], v[106:107], v[42:43] op_sel_hi:[0,1,1]
	v_pk_fma_f32 v[62:63], v[26:27], v[114:115], v[68:69] op_sel_hi:[0,1,1]
	v_pk_fma_f32 v[48:49], v[26:27], v[78:79], v[48:49] op_sel_hi:[0,1,1]
	v_pk_fma_f32 v[64:65], v[26:27], v[110:111], v[70:71] op_sel_hi:[0,1,1]
	v_pk_fma_f32 v[46:47], v[26:27], v[112:113], v[46:47] op_sel_hi:[0,1,1]
	v_pk_fma_f32 v[66:67], v[26:27], v[120:121], v[72:73] op_sel_hi:[0,1,1]
	v_pk_fma_f32 v[36:37], v[26:27], v[116:117], v[36:37] op_sel_hi:[0,1,1]
	v_pk_fma_f32 v[34:35], v[26:27], v[118:119], v[34:35] op_sel_hi:[0,1,1]
	v_pk_fma_f32 v[38:39], v[24:25], v[124:125], v[38:39] op_sel_hi:[0,1,1]
	v_pk_fma_f32 v[52:53], v[22:23], v[146:147], v[52:53] op_sel_hi:[0,1,1]
	v_pk_fma_f32 v[58:59], v[24:25], v[88:89], v[58:59] op_sel_hi:[0,1,1]
	v_pk_fma_f32 v[56:57], v[24:25], v[126:127], v[56:57] op_sel_hi:[0,1,1]
	v_pk_fma_f32 v[40:41], v[24:25], v[82:83], v[40:41] op_sel_hi:[0,1,1]
	v_pk_fma_f32 v[54:55], v[24:25], v[132:133], v[54:55] op_sel_hi:[0,1,1]
	v_pk_fma_f32 v[44:45], v[24:25], v[84:85], v[44:45] op_sel_hi:[0,1,1]
	v_pk_fma_f32 v[60:61], v[24:25], v[128:129], v[60:61] op_sel_hi:[0,1,1]
	v_pk_fma_f32 v[42:43], v[24:25], v[130:131], v[42:43] op_sel_hi:[0,1,1]
	v_pk_fma_f32 v[62:63], v[24:25], v[138:139], v[62:63] op_sel_hi:[0,1,1]
	v_pk_fma_f32 v[48:49], v[24:25], v[86:87], v[48:49] op_sel_hi:[0,1,1]
	v_pk_fma_f32 v[64:65], v[24:25], v[134:135], v[64:65] op_sel_hi:[0,1,1]
	v_pk_fma_f32 v[46:47], v[24:25], v[136:137], v[46:47] op_sel_hi:[0,1,1]
	v_pk_fma_f32 v[66:67], v[24:25], v[144:145], v[66:67] op_sel_hi:[0,1,1]
	v_pk_fma_f32 v[36:37], v[24:25], v[140:141], v[36:37] op_sel_hi:[0,1,1]
	v_pk_fma_f32 v[34:35], v[24:25], v[142:143], v[34:35] op_sel_hi:[0,1,1]
	v_pk_fma_f32 v[38:39], v[22:23], v[148:149], v[38:39] op_sel_hi:[0,1,1]
	v_pk_fma_f32 v[52:53], v[20:21], v[170:171], v[52:53] op_sel_hi:[0,1,1]
	v_pk_fma_f32 v[58:59], v[22:23], v[96:97], v[58:59] op_sel_hi:[0,1,1]
	v_pk_fma_f32 v[56:57], v[22:23], v[150:151], v[56:57] op_sel_hi:[0,1,1]
	v_pk_fma_f32 v[40:41], v[22:23], v[90:91], v[40:41] op_sel_hi:[0,1,1]
	v_pk_fma_f32 v[54:55], v[22:23], v[156:157], v[54:55] op_sel_hi:[0,1,1]
	v_pk_fma_f32 v[44:45], v[22:23], v[92:93], v[44:45] op_sel_hi:[0,1,1]
	v_pk_fma_f32 v[60:61], v[22:23], v[152:153], v[60:61] op_sel_hi:[0,1,1]
	v_pk_fma_f32 v[42:43], v[22:23], v[154:155], v[42:43] op_sel_hi:[0,1,1]
	v_pk_fma_f32 v[62:63], v[22:23], v[162:163], v[62:63] op_sel_hi:[0,1,1]
	v_pk_fma_f32 v[48:49], v[22:23], v[94:95], v[48:49] op_sel_hi:[0,1,1]
	v_pk_fma_f32 v[64:65], v[22:23], v[158:159], v[64:65] op_sel_hi:[0,1,1]
	v_pk_fma_f32 v[46:47], v[22:23], v[160:161], v[46:47] op_sel_hi:[0,1,1]
	v_pk_fma_f32 v[66:67], v[22:23], v[168:169], v[66:67] op_sel_hi:[0,1,1]
	v_pk_fma_f32 v[36:37], v[22:23], v[164:165], v[36:37] op_sel_hi:[0,1,1]
	v_pk_fma_f32 v[34:35], v[22:23], v[166:167], v[34:35] op_sel_hi:[0,1,1]
	v_pk_fma_f32 v[38:39], v[20:21], v[172:173], v[38:39] op_sel_hi:[0,1,1]
	v_pk_mul_f32 v[72:73], v[52:53], v[52:53]
	v_pk_fma_f32 v[50:51], v[20:21], v[50:51], v[58:59] op_sel_hi:[0,1,1]
	v_pk_fma_f32 v[56:57], v[20:21], v[174:175], v[56:57] op_sel_hi:[0,1,1]
	v_pk_fma_f32 v[40:41], v[20:21], v[98:99], v[40:41] op_sel_hi:[0,1,1]
	v_pk_fma_f32 v[54:55], v[20:21], v[180:181], v[54:55] op_sel_hi:[0,1,1]
	v_pk_fma_f32 v[44:45], v[20:21], v[100:101], v[44:45] op_sel_hi:[0,1,1]
	v_pk_fma_f32 v[58:59], v[20:21], v[176:177], v[60:61] op_sel_hi:[0,1,1]
	v_pk_fma_f32 v[42:43], v[20:21], v[178:179], v[42:43] op_sel_hi:[0,1,1]
	v_pk_fma_f32 v[60:61], v[20:21], v[186:187], v[62:63] op_sel_hi:[0,1,1]
	v_pk_fma_f32 v[48:49], v[20:21], v[102:103], v[48:49] op_sel_hi:[0,1,1]
	v_pk_fma_f32 v[62:63], v[20:21], v[182:183], v[64:65] op_sel_hi:[0,1,1]
	v_pk_fma_f32 v[46:47], v[20:21], v[184:185], v[46:47] op_sel_hi:[0,1,1]
	v_pk_fma_f32 v[64:65], v[20:21], v[192:193], v[66:67] op_sel_hi:[0,1,1]
	v_pk_fma_f32 v[36:37], v[20:21], v[188:189], v[36:37] op_sel_hi:[0,1,1]
	v_pk_fma_f32 v[34:35], v[20:21], v[190:191], v[34:35] op_sel_hi:[0,1,1]
	v_pk_mul_f32 v[74:75], v[38:39], v[38:39]
	v_add_f32_e32 v20, v72, v73
	v_add_f32_e32 v20, v20, v74
	v_pk_mul_f32 v[68:69], v[56:57], v[56:57]
	v_add_f32_e32 v20, v75, v20
	v_add_f32_e32 v20, v68, v20
	v_pk_mul_f32 v[70:71], v[40:41], v[40:41]
	v_add_f32_e32 v20, v69, v20
	v_add_f32_e32 v20, v70, v20
	v_pk_mul_f32 v[80:81], v[58:59], v[58:59]
	v_add_f32_e32 v20, v71, v20
	v_add_f32_e32 v20, v80, v20
	v_pk_mul_f32 v[82:83], v[42:43], v[42:43]
	v_add_f32_e32 v20, v81, v20
	v_add_f32_e32 v20, v82, v20
	v_pk_mul_f32 v[76:77], v[54:55], v[54:55]
	v_add_f32_e32 v20, v83, v20
	v_add_f32_e32 v20, v76, v20
	v_pk_mul_f32 v[78:79], v[44:45], v[44:45]
	v_add_f32_e32 v20, v77, v20
	v_add_f32_e32 v20, v78, v20
	v_pk_mul_f32 v[88:89], v[62:63], v[62:63]
	v_add_f32_e32 v20, v79, v20
	v_add_f32_e32 v20, v88, v20
	v_pk_mul_f32 v[90:91], v[46:47], v[46:47]
	v_add_f32_e32 v20, v89, v20
	v_add_f32_e32 v20, v90, v20
	v_pk_mul_f32 v[84:85], v[60:61], v[60:61]
	v_add_f32_e32 v20, v91, v20
	v_add_f32_e32 v20, v84, v20
	v_pk_mul_f32 v[86:87], v[48:49], v[48:49]
	v_add_f32_e32 v20, v85, v20
	v_add_f32_e32 v20, v86, v20
	v_pk_mul_f32 v[94:95], v[36:37], v[36:37]
	v_add_f32_e32 v20, v87, v20
	v_add_f32_e32 v20, v94, v20
	v_pk_mul_f32 v[96:97], v[34:35], v[34:35]
	v_add_f32_e32 v20, v95, v20
	v_add_f32_e32 v20, v96, v20
	v_pk_mul_f32 v[92:93], v[64:65], v[64:65]
	v_add_f32_e32 v20, v97, v20
	v_add_f32_e32 v20, v92, v20
	v_pk_mul_f32 v[66:67], v[50:51], v[50:51]
	v_add_f32_e32 v20, v93, v20
	v_add_f32_e32 v20, v66, v20
	v_add_f32_e32 v20, v67, v20
	ds_bpermute_b32 v22, v21, v20
	s_waitcnt lgkmcnt(0)
	v_add_f32_e32 v20, v20, v22
	ds_bpermute_b32 v22, v23, v20
	s_waitcnt lgkmcnt(0)
	v_add_f32_e32 v20, v20, v22
	ds_bpermute_b32 v22, v25, v20
	s_waitcnt lgkmcnt(0)
	v_add_f32_e32 v20, v20, v22
	ds_bpermute_b32 v22, v27, v20
	s_waitcnt lgkmcnt(0)
	v_add_f32_e32 v20, v20, v22
	ds_bpermute_b32 v22, v28, v20
	s_waitcnt lgkmcnt(0)
	v_add_f32_e32 v20, v20, v22
	ds_bpermute_b32 v22, v29, v20
	s_waitcnt lgkmcnt(0)
	v_add_f32_e32 v20, v20, v22
	v_fmamk_f32 v20, v20, 0x3a000000, v31
	v_mul_f32_e32 v22, 0x4f800000, v20
	v_cmp_gt_f32_e32 vcc, s16, v20
	s_nop 1
	v_cndmask_b32_e32 v20, v20, v22, vcc
	v_sqrt_f32_e32 v22, v20
	s_nop 0
	v_add_u32_e32 v24, -1, v22
	v_add_u32_e32 v26, 1, v22
	v_fma_f32 v33, -v24, v22, v20
	v_fma_f32 v66, -v26, v22, v20
	v_cmp_ge_f32_e64 s[0:1], 0, v33
	s_nop 1
	v_cndmask_b32_e64 v22, v22, v24, s[0:1]
	v_cmp_lt_f32_e64 s[0:1], 0, v66
	s_nop 1
	v_cndmask_b32_e64 v22, v22, v26, s[0:1]
	v_mul_f32_e32 v24, 0x37800000, v22
	v_cndmask_b32_e32 v22, v22, v24, vcc
	v_cmp_class_f32_e32 vcc, v20, v32
	s_nop 1
	v_cndmask_b32_e32 v20, v22, v20, vcc
	v_div_scale_f32 v22, s[0:1], v20, v20, 1.0
	v_rcp_f32_e32 v26, v22
	v_div_scale_f32 v24, vcc, 1.0, v20, 1.0
	v_fma_f32 v33, -v22, v26, 1.0
	v_fmac_f32_e32 v26, v33, v26
	v_mul_f32_e32 v33, v24, v26
	v_fma_f32 v66, -v22, v33, v24
	v_fmac_f32_e32 v33, v66, v26
	v_fma_f32 v22, -v22, v33, v24
	v_div_fmas_f32 v22, v22, v26, v33
	v_div_fixup_f32 v20, v22, v20, 1.0
	v_pk_mul_f32 v[52:53], v[52:53], v[20:21] op_sel_hi:[1,0]
	v_pk_mul_f32 v[38:39], v[38:39], v[20:21] op_sel_hi:[1,0]
	v_pk_mul_f32 v[56:57], v[56:57], v[20:21] op_sel_hi:[1,0]
	v_pk_mul_f32 v[40:41], v[40:41], v[20:21] op_sel_hi:[1,0]
	v_pk_mul_f32 v[6:7], v[6:7], v[38:39]
	v_pk_mul_f32 v[4:5], v[4:5], v[52:53]
	v_pk_mul_f32 v[2:3], v[2:3], v[40:41]
	v_pk_mul_f32 v[0:1], v[0:1], v[56:57]
	global_store_dwordx4 v[18:19], v[4:7], off offset:-4096
	global_store_dwordx4 v[18:19], v[0:3], off offset:-4080
	s_nop 1
	v_mov_b32_e32 v0, v208
	v_mov_b32_e32 v1, v209
	v_mov_b32_e32 v2, v210
	v_mov_b32_e32 v3, v211
	s_nop 0
	v_mov_b32_e32 v4, v212
	v_mov_b32_e32 v5, v213
	v_mov_b32_e32 v6, v214
	v_mov_b32_e32 v7, v215
	v_pk_mul_f32 v[38:39], v[42:43], v[20:21] op_sel_hi:[1,0]
	v_pk_mul_f32 v[40:41], v[58:59], v[20:21] op_sel_hi:[1,0]
	v_pk_mul_f32 v[42:43], v[44:45], v[20:21] op_sel_hi:[1,0]
	v_pk_mul_f32 v[44:45], v[54:55], v[20:21] op_sel_hi:[1,0]
	v_pk_mul_f32 v[34:35], v[34:35], v[20:21] op_sel_hi:[1,0]
	v_pk_mul_f32 v[36:37], v[36:37], v[20:21] op_sel_hi:[1,0]
	s_nop 0
	v_pk_mul_f32 v[0:1], v[0:1], v[40:41]
	v_pk_mul_f32 v[2:3], v[2:3], v[38:39]
	s_nop 0
	v_pk_mul_f32 v[4:5], v[4:5], v[44:45]
	v_pk_mul_f32 v[6:7], v[6:7], v[42:43]
	global_store_dwordx4 v[18:19], v[0:3], off offset:-2048
	global_store_dwordx4 v[18:19], v[4:7], off offset:-2032
	s_nop 1
	v_mov_b32_e32 v0, v216
	v_mov_b32_e32 v1, v217
	v_mov_b32_e32 v2, v218
	v_mov_b32_e32 v3, v219
	s_nop 0
	v_mov_b32_e32 v4, v220
	v_mov_b32_e32 v5, v221
	v_mov_b32_e32 v6, v222
	v_mov_b32_e32 v7, v223
	v_pk_mul_f32 v[38:39], v[46:47], v[20:21] op_sel_hi:[1,0]
	v_pk_mul_f32 v[40:41], v[62:63], v[20:21] op_sel_hi:[1,0]
	v_pk_mul_f32 v[42:43], v[48:49], v[20:21] op_sel_hi:[1,0]
	v_pk_mul_f32 v[44:45], v[60:61], v[20:21] op_sel_hi:[1,0]
	s_nop 0
	v_pk_mul_f32 v[0:1], v[0:1], v[40:41]
	v_pk_mul_f32 v[2:3], v[2:3], v[38:39]
	s_nop 0
	v_pk_mul_f32 v[4:5], v[4:5], v[44:45]
	v_pk_mul_f32 v[6:7], v[6:7], v[42:43]
	global_store_dwordx4 v[18:19], v[0:3], off
	global_store_dwordx4 v[18:19], v[4:7], off offset:16
	s_nop 1
	v_mov_b32_e32 v0, v224
	v_mov_b32_e32 v1, v225
	v_mov_b32_e32 v2, v226
	v_mov_b32_e32 v3, v227
	s_nop 0
	v_mov_b32_e32 v4, v228
	v_mov_b32_e32 v5, v229
	v_mov_b32_e32 v6, v230
	v_mov_b32_e32 v7, v231
	v_pk_mul_f32 v[38:39], v[50:51], v[20:21] op_sel_hi:[1,0]
	v_pk_mul_f32 v[40:41], v[64:65], v[20:21] op_sel_hi:[1,0]
	s_nop 0
	v_pk_mul_f32 v[0:1], v[0:1], v[36:37]
	v_pk_mul_f32 v[2:3], v[2:3], v[34:35]
	s_nop 0
	v_pk_mul_f32 v[4:5], v[4:5], v[40:41]
	v_pk_mul_f32 v[6:7], v[6:7], v[38:39]
	global_store_dwordx4 v[18:19], v[0:3], off offset:2048
	global_store_dwordx4 v[18:19], v[4:7], off offset:2064
	v_lshl_add_u64 v[18:19], v[18:19], 0, s[6:7]
	s_cbranch_scc1 .LBB0_1506
